# GLA-local output stores (QD/OI/DST/DEC) made non-temporal, so they do not evict the attention units' shared K/V bands under the phase-3 order swap
# baseline (speedup 1.0000x reference)
; #define LAS __attribute__((address_space(3)))
; __device__ __forceinline__ unsigned f2bf(float f) { unsigned u = __builtin_bit_cast(unsigned, f); return (u + 0x7fffu + ((u >> 16) & 1u)) >> 16; }
; __device__ __forceinline__ void gla_local_unit(LAS unsigned char* lds, GlaPre& R, const bf16_t* proj, const float* alow, const float (&w2)[16], const float bias, ...
;     ...
;     for (int x = 0; x < 2; ++x) { const int id = 2 * wave + x, ti = id >> 2, tj = id & 3; f32x4 acc = (f32x4){0.f, 0.f, 0.f, 0.f};
;         if (tj <= ti) {
; #pragma unroll
;             for (int ks = 0; ks < 4; ++ks) { const bf16x8 af = *(const LAS bf16x8*)(QD + (16 * ti + fr) * 272 + (32 * ks + 8 * fq) * 2); const bf16x8 bfr = *(const LAS bf16x8*)(KI + (16 * tj + fr) * 272 + (32 * ks + 8 * fq) * 2);
;                 acc = __builtin_amdgcn_mfma_f32_16x16x32_bf16(af, bfr, acc, 0, 0, 0); } }
; #pragma unroll
;         for (int rg = 0; rg < 4; ++rg) { const int i = 16 * ti + 4 * fq + rg, j = 16 * tj + fr; const float vv = (i >= j) ? acc[rg] : 0.f; *(LAS bf16_t*)(AT + i * 144 + 2 * j) = (bf16_t)f2bf(vv); } }
;     bf16x8 vfr[2][2];
;     { const int li = lane & 15, qq = li >> 2, pp = li & 3;
; #pragma unroll
;         for (int tv = 0; tv < 2; ++tv)
; #pragma unroll
;             for (int ks = 0; ks < 2; ++ks) { const int vt = 2 * wave + tv;
;                 const int r0 = 32 * ks + 8 * fq + qq, r1 = r0 + 4;
;                 const s16x4 a0 = vtr(VL + swz512(r0, 2 * vt + (pp >> 1)) + 8 * (pp & 1)), a1 = vtr(VL + swz512(r1, 2 * vt + (pp >> 1)) + 8 * (pp & 1));
;                 bf16x8 f; f[0] = a0[0]; f[1] = a0[1]; f[2] = a0[2]; f[3] = a0[3]; f[4] = a1[0]; f[5] = a1[1]; f[6] = a1[2]; f[7] = a1[3]; vfr[tv][ks] = f; } }
; #pragma unroll
;     for (int dt = 0; dt < 8; ++dt) {
;         bf16x8 kf[2];
; #pragma unroll
;         for (int ks = 0; ks < 2; ++ks) kf[ks] = *(const LAS bf16x8*)(KET + (16 * dt + fr) * 144 + (32 * ks + 8 * fq) * 2);
; #pragma unroll
;         for (int tv = 0; tv < 2; ++tv) { f32x4 acc = (f32x4){0.f, 0.f, 0.f, 0.f};
; #pragma unroll
;             for (int ks = 0; ks < 2; ++ks) acc = __builtin_amdgcn_mfma_f32_16x16x32_bf16(kf[ks], vfr[tv][ks], acc, 0, 0, 0);
;             u32x2 w; w.x = pk2(acc[0], acc[1]); w.y = pk2(acc[2], acc[3]);
;             *(u32x2*)(dstg + (((size_t)(b * 4 + h) * 8 + wave) * 32 + n) * 4096 + (size_t)(((dt * 2 + tv) * 64 + fr * 4 + fq) * 4)) = w; } }
.LBB0_349:
	s_nop 6
	v_cndmask_b32_e64 v0, v0, 0, s[22:23]
	v_bfe_u32 v4, v0, 16, 1
	v_add3_u32 v0, v0, v4, s33
	ds_write_b16_d16_hi v81, v0
	v_cndmask_b32_e64 v0, v1, 0, s[24:25]
	v_bfe_u32 v1, v0, 16, 1
	v_add3_u32 v0, v0, v1, s33
	ds_write_b16_d16_hi v81, v0 offset:144
	v_cndmask_b32_e64 v0, v2, 0, s[26:27]
	v_bfe_u32 v1, v0, 16, 1
	v_add3_u32 v0, v0, v1, s33
	ds_write_b16_d16_hi v81, v0 offset:288
	v_cndmask_b32_e64 v0, v3, 0, s[28:29]
	v_bfe_u32 v1, v0, 16, 1
	v_add3_u32 v0, v0, v1, s33
	ds_write_b16_d16_hi v81, v0 offset:432
	v_add_u32_e32 v0, v70, v69
	ds_read_b64_tr_b16 v[12:13], v0 offset:53248
	ds_read_b64_tr_b16 v[14:15], v82 offset:53248
	v_add_u32_e32 v0, v70, v71
	ds_read_b64_tr_b16 v[8:9], v0 offset:53248
	ds_read_b64_tr_b16 v[10:11], v83 offset:53248
	v_add_u32_e32 v0, v72, v69
	ds_read_b64_tr_b16 v[4:5], v0 offset:53248
	ds_read_b64_tr_b16 v[6:7], v84 offset:53248
	v_add_u32_e32 v0, v72, v71
	ds_read_b64_tr_b16 v[0:1], v0 offset:53248
	ds_read_b64_tr_b16 v[2:3], v85 offset:53248
	ds_read_b128 v[92:95], v86 offset:34816
	ds_read_b128 v[96:99], v86 offset:34880
	s_waitcnt lgkmcnt(1)
	v_mfma_f32_16x16x32_bf16 v[100:103], v[92:95], v[12:15], 0
	s_lshl_b64 s[2:3], s[2:3], 8
	v_readlane_b32 s30, v253, 19
	s_add_u32 s2, s2, s30
	v_mfma_f32_16x16x32_bf16 v[92:95], v[92:95], v[4:7], 0
	s_addc_u32 s3, s3, 0
	s_or_b32 s2, s2, s31
	s_lshl_b64 s[30:31], s[2:3], 13
	s_waitcnt lgkmcnt(0)
	v_mfma_f32_16x16x32_bf16 v[100:103], v[96:99], v[8:11], v[100:103]
	v_lshl_add_u64 v[44:45], v[38:39], 0, s[30:31]
	s_lshl_b64 s[2:3], s[2:3], 12
	s_add_i32 s41, s41, s74
	v_mfma_f32_16x16x32_bf16 v[92:95], v[96:99], v[0:3], v[92:95]
	s_nop 3
	v_cvt_pk_bf16_f32 v100, v100, v101
	v_cvt_pk_bf16_f32 v101, v102, v103
	s_nop 1
	v_cvt_pk_bf16_f32 v92, v92, v93
	v_cvt_pk_bf16_f32 v93, v94, v95
	global_store_dwordx2 v[44:45], v[100:101], off nt
	global_store_dwordx2 v[44:45], v[92:93], off offset:512 nt
	ds_read_b128 v[92:95], v86 offset:37120
	ds_read_b128 v[96:99], v86 offset:37184
	s_waitcnt lgkmcnt(1)
	v_mfma_f32_16x16x32_bf16 v[100:103], v[92:95], v[12:15], 0
	v_mfma_f32_16x16x32_bf16 v[92:95], v[92:95], v[4:7], 0
	s_waitcnt lgkmcnt(0)
	v_mfma_f32_16x16x32_bf16 v[100:103], v[96:99], v[8:11], v[100:103]
	v_mfma_f32_16x16x32_bf16 v[92:95], v[96:99], v[0:3], v[92:95]
	s_nop 6
	v_cvt_pk_bf16_f32 v100, v100, v101
	v_cvt_pk_bf16_f32 v101, v102, v103
	v_cvt_pk_bf16_f32 v92, v92, v93
	v_cvt_pk_bf16_f32 v93, v94, v95
	global_store_dwordx2 v[44:45], v[100:101], off offset:1024 nt
	global_store_dwordx2 v[44:45], v[92:93], off offset:1536 nt
	ds_read_b128 v[92:95], v86 offset:39424
	ds_read_b128 v[96:99], v86 offset:39488
	s_waitcnt lgkmcnt(1)
	v_mfma_f32_16x16x32_bf16 v[100:103], v[92:95], v[12:15], 0
	v_mfma_f32_16x16x32_bf16 v[92:95], v[92:95], v[4:7], 0
	s_waitcnt lgkmcnt(0)
	v_mfma_f32_16x16x32_bf16 v[100:103], v[96:99], v[8:11], v[100:103]
	v_mfma_f32_16x16x32_bf16 v[92:95], v[96:99], v[0:3], v[92:95]
	s_nop 6
	v_cvt_pk_bf16_f32 v100, v100, v101
	v_cvt_pk_bf16_f32 v101, v102, v103
	v_cvt_pk_bf16_f32 v92, v92, v93
	v_cvt_pk_bf16_f32 v93, v94, v95
	global_store_dwordx2 v[44:45], v[100:101], off offset:2048 nt
	global_store_dwordx2 v[44:45], v[92:93], off offset:2560 nt
	ds_read_b128 v[92:95], v86 offset:41728
	ds_read_b128 v[96:99], v86 offset:41792
	s_waitcnt lgkmcnt(1)
	v_mfma_f32_16x16x32_bf16 v[100:103], v[92:95], v[12:15], 0
	v_mfma_f32_16x16x32_bf16 v[92:95], v[92:95], v[4:7], 0
	s_waitcnt lgkmcnt(0)
	v_mfma_f32_16x16x32_bf16 v[100:103], v[96:99], v[8:11], v[100:103]
	v_mfma_f32_16x16x32_bf16 v[92:95], v[96:99], v[0:3], v[92:95]
	s_nop 6
	v_cvt_pk_bf16_f32 v100, v100, v101
	v_cvt_pk_bf16_f32 v101, v102, v103
	v_cvt_pk_bf16_f32 v92, v92, v93
	v_cvt_pk_bf16_f32 v93, v94, v95
	global_store_dwordx2 v[44:45], v[100:101], off offset:3072 nt
	global_store_dwordx2 v[44:45], v[92:93], off offset:3584 nt
	ds_read_b128 v[92:95], v86 offset:44032
	ds_read_b128 v[96:99], v86 offset:44096
	s_waitcnt lgkmcnt(1)
	v_mfma_f32_16x16x32_bf16 v[100:103], v[92:95], v[12:15], 0
	v_add_co_u32_e32 v44, vcc, s82, v44
	v_mfma_f32_16x16x32_bf16 v[92:95], v[92:95], v[4:7], 0
	s_nop 0
	v_addc_co_u32_e32 v45, vcc, 0, v45, vcc
	s_waitcnt lgkmcnt(0)
	v_mfma_f32_16x16x32_bf16 v[100:103], v[96:99], v[8:11], v[100:103]
	v_mfma_f32_16x16x32_bf16 v[92:95], v[96:99], v[0:3], v[92:95]
	s_nop 6
	v_cvt_pk_bf16_f32 v100, v100, v101
	v_cvt_pk_bf16_f32 v101, v102, v103
	v_cvt_pk_bf16_f32 v92, v92, v93
	v_cvt_pk_bf16_f32 v93, v94, v95
	global_store_dwordx2 v[44:45], v[100:101], off nt
	global_store_dwordx2 v[44:45], v[92:93], off offset:512 nt
	ds_read_b128 v[92:95], v86 offset:46336
	ds_read_b128 v[96:99], v86 offset:46400
	s_waitcnt lgkmcnt(1)
	v_mfma_f32_16x16x32_bf16 v[100:103], v[92:95], v[12:15], 0
	v_mfma_f32_16x16x32_bf16 v[92:95], v[92:95], v[4:7], 0
	s_waitcnt lgkmcnt(0)
	v_mfma_f32_16x16x32_bf16 v[100:103], v[96:99], v[8:11], v[100:103]
	v_mfma_f32_16x16x32_bf16 v[92:95], v[96:99], v[0:3], v[92:95]
	s_nop 6
	v_cvt_pk_bf16_f32 v100, v100, v101
	v_cvt_pk_bf16_f32 v101, v102, v103
	v_cvt_pk_bf16_f32 v92, v92, v93
	v_cvt_pk_bf16_f32 v93, v94, v95
	global_store_dwordx2 v[44:45], v[100:101], off offset:1024 nt
	global_store_dwordx2 v[44:45], v[92:93], off offset:1536 nt
	ds_read_b128 v[92:95], v86 offset:48640
	ds_read_b128 v[96:99], v86 offset:48704
	s_waitcnt lgkmcnt(1)
	v_mfma_f32_16x16x32_bf16 v[100:103], v[92:95], v[12:15], 0
	v_mfma_f32_16x16x32_bf16 v[92:95], v[92:95], v[4:7], 0
	s_waitcnt lgkmcnt(0)
	v_mfma_f32_16x16x32_bf16 v[100:103], v[96:99], v[8:11], v[100:103]
	v_mfma_f32_16x16x32_bf16 v[92:95], v[96:99], v[0:3], v[92:95]
	s_nop 6
	v_cvt_pk_bf16_f32 v100, v100, v101
	v_cvt_pk_bf16_f32 v101, v102, v103
	v_cvt_pk_bf16_f32 v92, v92, v93
	v_cvt_pk_bf16_f32 v93, v94, v95
	global_store_dwordx2 v[44:45], v[100:101], off offset:2048 nt
	global_store_dwordx2 v[44:45], v[92:93], off offset:2560 nt
	ds_read_b128 v[92:95], v86 offset:50944
	ds_read_b128 v[96:99], v86 offset:51008
	s_waitcnt lgkmcnt(1)
	v_mfma_f32_16x16x32_bf16 v[100:103], v[92:95], v[12:15], 0
	v_mfma_f32_16x16x32_bf16 v[92:95], v[92:95], v[4:7], 0
	s_waitcnt lgkmcnt(0)
	v_mfma_f32_16x16x32_bf16 v[100:103], v[96:99], v[8:11], v[100:103]
	v_mfma_f32_16x16x32_bf16 v[92:95], v[96:99], v[0:3], v[92:95]
	s_nop 6
	v_cvt_pk_bf16_f32 v100, v100, v101
	v_cvt_pk_bf16_f32 v101, v102, v103
	v_cvt_pk_bf16_f32 v92, v92, v93
	v_cvt_pk_bf16_f32 v93, v94, v95
	global_store_dwordx2 v[44:45], v[100:101], off offset:3072 nt
	global_store_dwordx2 v[44:45], v[92:93], off offset:3584 nt
	s_barrier
; __device__ __forceinline__ void gla_local_issue(GlaPre& R, const bf16_t* proj, const float* alow, int u, int tid) {
;     const int n = u & 31, h = (u >> 5) & 3, b = u >> 7;
;     const size_t t0 = (size_t)b * SEQ + 64 * n;
;     R.al0 = alow[t0 * 16 + tid]; R.al1 = alow[t0 * 16 + 512 + tid];
; #pragma unroll
;     for (int it = 0; it < 2; ++it) { const int id = tid + NTHREADS * it, row = id >> 4, ch = id & 15; const bf16_t* src = proj + (t0 + row) * NP + h * 128 + ch * 8; R.q[it] = *(const u32x4*)(src + QB); R.k[it] = *(const u32x4*)(src + KB); }
; #pragma unroll
;     for (int it = 0; it < 4; ++it) { const int id = tid + NTHREADS * it, row = id >> 5, ch = id & 31; R.v[it] = *(const u32x4*)(proj + (t0 + row) * NP + VB + h * 256 + ch * 8); }
; }
; __device__ __forceinline__ void gla_local_unit(LAS unsigned char* lds, GlaPre& R, const bf16_t* proj, const float* alow, const float (&w2)[16], const float bias, ...
;     const int n = u & 31, h = (u >> 5) & 3, b = u >> 7;
;     const int d = tid & 127, ig = tid >> 7;
;     const int fr = lane & 15, fq = lane >> 4;
;     LAS unsigned char* QD = lds; LAS unsigned char* KI = lds + 17408; LAS unsigned char* KET = lds + 34816; LAS unsigned char* VL = lds + 53248;
;     LAS unsigned char* AT = lds + 86016;
;     LAS float* CS = (LAS float*)(lds + 95232); LAS float* ALs = (LAS float*)(lds + 97280);
;     const size_t t0 = (size_t)b * SEQ + 64 * n;
; #pragma unroll
;     for (int it = 0; it < 2; ++it) { const int id = tid + NTHREADS * it, row = id >> 4, ch = id & 15; *(LAS u32x4*)(QD + row * 272 + ch * 16) = R.q[it]; *(LAS u32x4*)(KI + row * 272 + ch * 16) = R.k[it]; }
;     ALs[tid] = R.al0; ALs[512 + tid] = R.al1;
;     ...
;     __syncthreads();
; #pragma unroll
;     for (int ti = 0; ti < 4; ++ti) {
;         bf16x8 af[2];
; #pragma unroll
;         for (int ks = 0; ks < 2; ++ks) af[ks] = *(const LAS bf16x8*)(AT + (16 * ti + fr) * 144 + (32 * ks + 8 * fq) * 2);
; #pragma unroll
;         for (int tv = 0; tv < 2; ++tv) { f32x4 acc = (f32x4){0.f, 0.f, 0.f, 0.f};
; #pragma unroll
;             for (int ks = 0; ks < 2; ++ks) acc = __builtin_amdgcn_mfma_f32_16x16x32_bf16(vfr[tv][ks], af[ks], acc, 0, 0, 0);
;             u32x2 w; w.x = pk2(acc[0], acc[1]); w.y = pk2(acc[2], acc[3]);
;             *(u32x2*)(oig + (((size_t)(b * 4 + h) * 8 + wave) * 32 + n) * 2048 + (size_t)(((ti * 2 + tv) * 64 + fr * 4 + fq) * 4)) = w; } }
	ds_read_b128 v[92:95], v87
	ds_read_b128 v[96:99], v87 offset:64
	s_waitcnt lgkmcnt(1)
	v_mfma_f32_16x16x32_bf16 v[100:103], v[12:15], v[92:95], 0
	v_lshl_add_u64 v[44:45], v[40:41], 0, s[2:3]
	v_readlane_b32 s2, v254, 22
	s_add_i32 s40, s40, s2
	v_mfma_f32_16x16x32_bf16 v[92:95], v[4:7], v[92:95], 0
	v_readlane_b32 s2, v254, 59
	v_readlane_b32 s3, v254, 60
	s_cmpk_gt_i32 s41, 0x3ff
	s_waitcnt lgkmcnt(0)
	v_mfma_f32_16x16x32_bf16 v[100:103], v[8:11], v[96:99], v[100:103]
	v_lshl_add_u64 v[42:43], v[42:43], 0, s[2:3]
	v_mfma_f32_16x16x32_bf16 v[92:95], v[0:3], v[96:99], v[92:95]
	s_nop 5
	v_cvt_pk_bf16_f32 v100, v100, v101
	v_cvt_pk_bf16_f32 v101, v102, v103
	v_cvt_pk_bf16_f32 v92, v92, v93
	v_cvt_pk_bf16_f32 v93, v94, v95
	global_store_dwordx2 v[44:45], v[100:101], off nt
	global_store_dwordx2 v[44:45], v[92:93], off offset:512 nt
	ds_read_b128 v[92:95], v87 offset:2304
	ds_read_b128 v[96:99], v87 offset:2368
	s_waitcnt lgkmcnt(1)
	v_mfma_f32_16x16x32_bf16 v[100:103], v[12:15], v[92:95], 0
	v_mfma_f32_16x16x32_bf16 v[92:95], v[4:7], v[92:95], 0
	s_waitcnt lgkmcnt(0)
	v_mfma_f32_16x16x32_bf16 v[100:103], v[8:11], v[96:99], v[100:103]
	v_mfma_f32_16x16x32_bf16 v[92:95], v[0:3], v[96:99], v[92:95]
	s_nop 6
	v_cvt_pk_bf16_f32 v100, v100, v101
	v_cvt_pk_bf16_f32 v101, v102, v103
	v_cvt_pk_bf16_f32 v92, v92, v93
	v_cvt_pk_bf16_f32 v93, v94, v95
	global_store_dwordx2 v[44:45], v[100:101], off offset:1024 nt
	global_store_dwordx2 v[44:45], v[92:93], off offset:1536 nt
	ds_read_b128 v[92:95], v87 offset:4608
	ds_read_b128 v[96:99], v87 offset:4672
	s_waitcnt lgkmcnt(1)
	v_mfma_f32_16x16x32_bf16 v[100:103], v[12:15], v[92:95], 0
	v_mfma_f32_16x16x32_bf16 v[92:95], v[4:7], v[92:95], 0
	s_waitcnt lgkmcnt(0)
	v_mfma_f32_16x16x32_bf16 v[100:103], v[8:11], v[96:99], v[100:103]
	v_mfma_f32_16x16x32_bf16 v[92:95], v[0:3], v[96:99], v[92:95]
	s_nop 6
	v_cvt_pk_bf16_f32 v100, v100, v101
	v_cvt_pk_bf16_f32 v101, v102, v103
	v_cvt_pk_bf16_f32 v92, v92, v93
	v_cvt_pk_bf16_f32 v93, v94, v95
	global_store_dwordx2 v[44:45], v[100:101], off offset:2048 nt
	global_store_dwordx2 v[44:45], v[92:93], off offset:2560 nt
	ds_read_b128 v[92:95], v87 offset:6912
	ds_read_b128 v[96:99], v87 offset:6976
	s_waitcnt lgkmcnt(1)
	v_mfma_f32_16x16x32_bf16 v[12:15], v[12:15], v[92:95], 0
	v_mfma_f32_16x16x32_bf16 v[4:7], v[4:7], v[92:95], 0
	s_waitcnt lgkmcnt(0)
	v_mfma_f32_16x16x32_bf16 v[8:11], v[8:11], v[96:99], v[12:15]
	v_mfma_f32_16x16x32_bf16 v[0:3], v[0:3], v[96:99], v[4:7]
	s_nop 6
	v_cvt_pk_bf16_f32 v8, v8, v9
	v_cvt_pk_bf16_f32 v9, v10, v11
	v_cvt_pk_bf16_f32 v0, v0, v1
	v_cvt_pk_bf16_f32 v1, v2, v3
	global_store_dwordx2 v[44:45], v[8:9], off offset:3072 nt
	global_store_dwordx2 v[44:45], v[0:1], off offset:3584 nt
	s_barrier
	s_cbranch_scc1 .LBB0_356
.LBB0_350:
	s_ashr_i32 s2, s41, 7
	s_ashr_i32 s3, s2, 31
	s_bfe_u32 s30, s41, 0x20005
	s_lshl_b64 s[2:3], s[2:3], 11
	s_and_b32 s31, s40, 0x7c0
	s_or_b32 s2, s2, s31
	s_lshl_b32 s96, s30, 8
	s_lshl_b64 s[34:35], s[2:3], 6
	v_lshl_add_u64 v[4:5], v[16:17], 0, s[96:97]
	v_lshl_add_u64 v[2:3], s[2:3], 0, v[18:19]
	v_lshl_add_u64 v[0:1], v[36:37], 0, s[34:35]
	v_mad_u64_u32 v[6:7], s[34:35], v2, s49, v[4:5]
	s_movk_i32 s31, 0x2000
	v_lshl_add_u64 v[14:15], s[2:3], 0, v[22:23]
	v_mov_b64_e32 v[44:45], s[0:1]
	v_mad_i32_i24 v2, v3, s49, v7
	v_add_co_u32_e32 v6, vcc, s31, v6
	v_lshl_add_u64 v[8:9], s[2:3], 0, v[20:21]
	v_mad_u64_u32 v[92:93], s[34:35], v14, s49, v[44:45]
	v_lshl_add_u64 v[96:97], s[2:3], 0, v[24:25]
	v_addc_co_u32_e32 v7, vcc, 0, v2, vcc
	v_mad_u64_u32 v[4:5], s[34:35], v8, s49, v[4:5]
	v_mad_i32_i24 v93, v15, s49, v93
	s_lshl_b32 s96, s30, 9
	v_mad_u64_u32 v[98:99], s[34:35], v96, s49, v[44:45]
	v_mad_i32_i24 v5, v9, s49, v5
	v_add_co_u32_e32 v12, vcc, s31, v4
	v_lshl_add_u64 v[14:15], v[92:93], 0, s[96:97]
	v_mad_i32_i24 v99, v97, s49, v99
	v_addc_co_u32_e32 v13, vcc, 0, v5, vcc
	v_lshl_add_u64 v[14:15], v[14:15], 0, v[32:33]
	v_lshl_add_u64 v[96:97], v[98:99], 0, s[96:97]
	v_lshl_add_u64 v[98:99], s[2:3], 0, v[26:27]
	v_add_co_u32_e32 v92, vcc, s31, v14
	v_mad_u64_u32 v[100:101], s[34:35], v98, s49, v[44:45]
	s_nop 0
	v_addc_co_u32_e32 v93, vcc, 0, v15, vcc
	v_lshl_add_u64 v[96:97], v[96:97], 0, v[32:33]
	v_mad_i32_i24 v101, v99, s49, v101
	v_add_co_u32_e32 v96, vcc, s31, v96
	v_lshl_add_u64 v[98:99], v[100:101], 0, s[96:97]
	s_nop 0
	v_addc_co_u32_e32 v97, vcc, 0, v97, vcc
	v_lshl_add_u64 v[98:99], v[98:99], 0, v[32:33]
	v_add_co_u32_e32 v100, vcc, s31, v98
	global_load_dword v91, v[0:1], off
	global_load_dword v108, v[0:1], off offset:2048
	s_nop 0
	global_load_dwordx4 v[0:3], v[6:7], off offset:1024
	v_addc_co_u32_e32 v101, vcc, 0, v99, vcc
	global_load_dwordx4 v[4:7], v[6:7], off offset:2048
	s_nop 0
	global_load_dwordx4 v[8:11], v[12:13], off offset:1024
	s_nop 0
	global_load_dwordx4 v[12:15], v[12:13], off offset:2048
	s_nop 0
	global_load_dwordx4 v[92:95], v[92:93], off offset:3072
	s_nop 0
	global_load_dwordx4 v[96:99], v[96:97], off offset:3072
	s_nop 0
	global_load_dwordx4 v[100:103], v[100:101], off offset:3072
	v_lshl_add_u64 v[104:105], s[2:3], 0, v[28:29]
	v_mad_u64_u32 v[44:45], s[2:3], v104, s49, v[44:45]
	v_mad_i32_i24 v45, v105, s49, v45
	v_lshl_add_u64 v[44:45], v[44:45], 0, s[96:97]
	v_lshl_add_u64 v[44:45], v[44:45], 0, v[32:33]
	v_add_co_u32_e32 v44, vcc, s31, v44
	s_mov_b32 s3, 0xbfb8aa3b
	s_nop 0
	v_addc_co_u32_e32 v45, vcc, 0, v45, vcc
	global_load_dwordx4 v[104:107], v[44:45], off offset:3072
	s_mov_b32 s31, 0x800000
	s_mov_b32 s42, 0x3f317217
	s_mov_b32 s43, 0x7f800000
	s_mov_b32 s2, 0x3d800000
	s_waitcnt vmcnt(7)
	ds_write_b128 v88, v[0:3]
	s_waitcnt vmcnt(6)
	ds_write_b128 v88, v[4:7] offset:17408
	s_waitcnt vmcnt(5)
	ds_write_b128 v89, v[8:11]
	s_waitcnt vmcnt(4)
	ds_write_b128 v89, v[12:15] offset:17408
	ds_write2st64_b32 v63, v91, v108 offset1:8
	s_waitcnt vmcnt(3)
	ds_write_b128 v73, v[92:95] offset:53248
	s_waitcnt vmcnt(2)
	ds_write_b128 v74, v[96:99] offset:53248
	s_waitcnt vmcnt(1)
	ds_write_b128 v75, v[100:103] offset:53248
	s_waitcnt vmcnt(0)
	ds_write_b128 v76, v[104:107] offset:53248
	s_waitcnt lgkmcnt(0)
	s_barrier
; #define LAS __attribute__((address_space(3)))
; __device__ __forceinline__ void gla_local_unit(LAS unsigned char* lds, GlaPre& R, const bf16_t* proj, const float* alow, const float (&w2)[16], const float bias, ...
;     ...
;     float bl[16]; float run = 0.f;
; #pragma unroll
;     for (int ii = 0; ii < 16; ++ii) { float z = bias; const LAS f32x4* ap = (const LAS f32x4*)(ALs + (16 * ig + ii) * 16);
; #pragma unroll
;         for (int r4 = 0; r4 < 4; ++r4) { const f32x4 av = ap[r4]; z = fmaf(av[0], w2[4 * r4], z); z = fmaf(av[1], w2[4 * r4 + 1], z); z = fmaf(av[2], w2[4 * r4 + 2], z); z = fmaf(av[3], w2[4 * r4 + 3], z); }
;         const float la = (fminf(z, 0.f) - __logf(1.0f + __expf(-fabsf(z)))) * 0.0625f; run += la; bl[ii] = run; }
	ds_read_b128 v[0:3], v64
	ds_read_b128 v[4:7], v64 offset:16
	ds_read_b128 v[8:11], v64 offset:32
	ds_read_b128 v[12:15], v64 offset:48
	ds_read_b128 v[92:95], v64 offset:64
	s_waitcnt lgkmcnt(4)
	v_fma_f32 v44, v0, v55, v61
	v_fmac_f32_e32 v44, v1, v56
	v_fmac_f32_e32 v44, v2, v46
	v_fmac_f32_e32 v44, v3, v57
	s_waitcnt lgkmcnt(3)
	v_fmac_f32_e32 v44, v4, v47
	v_fmac_f32_e32 v44, v5, v48
	v_fmac_f32_e32 v44, v6, v49
	v_fmac_f32_e32 v44, v7, v58
	s_waitcnt lgkmcnt(2)
	v_fmac_f32_e32 v44, v8, v50
	v_fmac_f32_e32 v44, v9, v51
	v_fmac_f32_e32 v44, v10, v52
	v_fmac_f32_e32 v44, v11, v59
	s_waitcnt lgkmcnt(1)
	v_fmac_f32_e32 v44, v12, v53
	v_fmac_f32_e32 v44, v13, v54
	v_fmac_f32_e32 v44, v14, v60
	v_fmac_f32_e32 v44, v15, v62
	v_mul_f32_e64 v0, |v44|, s3
	v_exp_f32_e32 v4, v0
	ds_read_b128 v[0:3], v64 offset:80
	s_waitcnt lgkmcnt(1)
	v_fma_f32 v8, v92, v55, v61
	v_fmac_f32_e32 v8, v93, v56
	v_add_f32_e32 v4, 1.0, v4
	v_cmp_gt_f32_e32 vcc, s31, v4
	v_fmac_f32_e32 v8, v94, v46
	v_fmac_f32_e32 v8, v95, v57
	v_cndmask_b32_e64 v5, 0, 32, vcc
	v_ldexp_f32 v4, v4, v5
	v_log_f32_e32 v9, v4
	v_min_f32_e32 v10, 0, v44
	ds_read_b128 v[92:95], v64 offset:592
	ds_read_b128 v[96:99], v64 offset:848
	v_mul_f32_e32 v4, 0x3f317217, v9
	v_fma_f32 v11, v9, s42, -v4
	ds_read_b128 v[4:7], v64 offset:96
	s_waitcnt lgkmcnt(3)
	v_fmac_f32_e32 v8, v0, v47
	v_fmac_f32_e32 v8, v1, v48
	v_fmac_f32_e32 v8, v2, v49
	v_fmac_f32_e32 v8, v3, v58
	ds_read_b128 v[0:3], v64 offset:112
	s_waitcnt lgkmcnt(1)
	v_fmac_f32_e32 v8, v4, v50
	v_fmac_f32_e32 v8, v5, v51
	v_fmac_f32_e32 v8, v6, v52
	v_fmac_f32_e32 v8, v7, v59
	ds_read_b128 v[4:7], v64 offset:128
	s_waitcnt lgkmcnt(1)
	v_fmac_f32_e32 v8, v0, v53
	v_fmac_f32_e32 v8, v1, v54
	v_fmac_f32_e32 v8, v2, v60
	v_fmac_f32_e32 v8, v3, v62
	v_mul_f32_e64 v0, |v8|, s3
	v_exp_f32_e32 v0, v0
	v_fmac_f32_e32 v11, 0x3377d1cf, v9
	v_fmac_f32_e32 v11, 0x3f317217, v9
	v_cmp_lt_f32_e64 s[34:35], |v9|, s43
	v_cndmask_b32_e32 v2, 0, v191, vcc
	v_add_f32_e32 v0, 1.0, v0
	v_cndmask_b32_e64 v1, v9, v11, s[34:35]
	v_sub_f32_e32 v1, v1, v2
	v_cmp_gt_f32_e32 vcc, s31, v0
	v_sub_f32_e32 v1, v10, v1
	s_waitcnt lgkmcnt(0)
	v_fma_f32 v12, v4, v55, v61
	v_cndmask_b32_e64 v2, 0, 32, vcc
	v_ldexp_f32 v0, v0, v2
	v_fma_f32 v2, v1, s2, 0
	v_min_f32_e32 v1, 0, v8
	ds_read_b128 v[8:11], v64 offset:144
	v_fmac_f32_e32 v12, v5, v56
	v_fmac_f32_e32 v12, v6, v46
	v_fmac_f32_e32 v12, v7, v57
	ds_read_b128 v[4:7], v64 offset:160
	s_waitcnt lgkmcnt(1)
	v_fmac_f32_e32 v12, v8, v47
	v_fmac_f32_e32 v12, v9, v48
	v_fmac_f32_e32 v12, v10, v49
	v_fmac_f32_e32 v12, v11, v58
	ds_read_b128 v[8:11], v64 offset:176
	s_waitcnt lgkmcnt(1)
	v_fmac_f32_e32 v12, v4, v50
	v_fmac_f32_e32 v12, v5, v51
	v_fmac_f32_e32 v12, v6, v52
	v_fmac_f32_e32 v12, v7, v59
	v_log_f32_e32 v0, v0
	s_waitcnt lgkmcnt(0)
	v_fmac_f32_e32 v12, v8, v53
	v_fmac_f32_e32 v12, v9, v54
	v_fmac_f32_e32 v12, v10, v60
	v_fmac_f32_e32 v12, v11, v62
	v_mul_f32_e32 v3, 0x3f317217, v0
	v_mul_f32_e64 v4, |v12|, s3
	v_fma_f32 v3, v0, s42, -v3
	v_exp_f32_e32 v4, v4
	v_fmac_f32_e32 v3, 0x3377d1cf, v0
	v_fmac_f32_e32 v3, 0x3f317217, v0
	v_cmp_lt_f32_e64 s[34:35], |v0|, s43
	s_mov_b32 s2, 0xffff0000
	s_nop 0
	v_cndmask_b32_e64 v0, v0, v3, s[34:35]
	v_cndmask_b32_e32 v3, 0, v191, vcc
	v_sub_f32_e32 v0, v0, v3
	v_add_f32_e32 v3, 1.0, v4
	v_cmp_gt_f32_e32 vcc, s31, v3
	v_sub_f32_e32 v0, v1, v0
	v_min_f32_e32 v1, 0, v12
	v_cndmask_b32_e64 v4, 0, 32, vcc
	v_ldexp_f32 v3, v3, v4
	v_log_f32_e32 v3, v3
	ds_read_b128 v[4:7], v64 offset:192
	v_fmamk_f32 v0, v0, 0x3d800000, v2
	v_mul_f32_e32 v8, 0x3f317217, v3
	v_fma_f32 v12, v3, s42, -v8
	ds_read_b128 v[8:11], v64 offset:208
	s_waitcnt lgkmcnt(1)
	v_fma_f32 v13, v4, v55, v61
	v_fmac_f32_e32 v13, v5, v56
	v_fmac_f32_e32 v13, v6, v46
	v_fmac_f32_e32 v13, v7, v57
	ds_read_b128 v[4:7], v64 offset:224
	s_waitcnt lgkmcnt(1)
	v_fmac_f32_e32 v13, v8, v47
	v_fmac_f32_e32 v13, v9, v48
	v_fmac_f32_e32 v13, v10, v49
	v_fmac_f32_e32 v13, v11, v58
	ds_read_b128 v[8:11], v64 offset:240
	s_waitcnt lgkmcnt(1)
	v_fmac_f32_e32 v13, v4, v50
	v_fmac_f32_e32 v13, v5, v51
	v_fmac_f32_e32 v13, v6, v52
	v_fmac_f32_e32 v13, v7, v59
	s_waitcnt lgkmcnt(0)
	v_fmac_f32_e32 v13, v8, v53
	v_fmac_f32_e32 v13, v9, v54
	v_fmac_f32_e32 v13, v10, v60
	v_fmac_f32_e32 v13, v11, v62
	v_mul_f32_e64 v4, |v13|, s3
	v_exp_f32_e32 v4, v4
	v_fmac_f32_e32 v12, 0x3377d1cf, v3
	v_fmac_f32_e32 v12, 0x3f317217, v3
	v_cmp_lt_f32_e64 s[34:35], |v3|, s43
	v_add_f32_e32 v4, 1.0, v4
	v_cndmask_b32_e32 v5, 0, v191, vcc
	v_cndmask_b32_e64 v3, v3, v12, s[34:35]
	v_cmp_gt_f32_e32 vcc, s31, v4
	v_sub_f32_e32 v3, v3, v5
	v_sub_f32_e32 v1, v1, v3
	v_cndmask_b32_e64 v5, 0, 32, vcc
	v_ldexp_f32 v4, v4, v5
	v_log_f32_e32 v12, v4
	ds_read_b128 v[4:7], v64 offset:256
	v_min_f32_e32 v3, 0, v13
	v_fmamk_f32 v1, v1, 0x3d800000, v0
	v_mul_f32_e32 v8, 0x3f317217, v12
	v_fma_f32 v13, v12, s42, -v8
	ds_read_b128 v[8:11], v64 offset:272
	s_waitcnt lgkmcnt(1)
	v_fma_f32 v14, v4, v55, v61
	v_fmac_f32_e32 v14, v5, v56
	v_fmac_f32_e32 v14, v6, v46
	v_fmac_f32_e32 v14, v7, v57
	ds_read_b128 v[4:7], v64 offset:288
	s_waitcnt lgkmcnt(1)
	v_fmac_f32_e32 v14, v8, v47
	v_fmac_f32_e32 v14, v9, v48
	v_fmac_f32_e32 v14, v10, v49
	v_fmac_f32_e32 v14, v11, v58
	ds_read_b128 v[8:11], v64 offset:304
	s_waitcnt lgkmcnt(1)
	v_fmac_f32_e32 v14, v4, v50
	v_fmac_f32_e32 v14, v5, v51
	v_fmac_f32_e32 v14, v6, v52
	v_fmac_f32_e32 v14, v7, v59
	s_waitcnt lgkmcnt(0)
; #define LAS __attribute__((address_space(3)))
; __device__ __forceinline__ void gla_local_unit(LAS unsigned char* lds, GlaPre& R, const bf16_t* proj, const float* alow, const float (&w2)[16], const float bias, ...
;     ...
;     float bl[16]; float run = 0.f;
; #pragma unroll
;     for (int ii = 0; ii < 16; ++ii) { float z = bias; const LAS f32x4* ap = (const LAS f32x4*)(ALs + (16 * ig + ii) * 16);
; #pragma unroll
;         for (int r4 = 0; r4 < 4; ++r4) { const f32x4 av = ap[r4]; z = fmaf(av[0], w2[4 * r4], z); z = fmaf(av[1], w2[4 * r4 + 1], z); z = fmaf(av[2], w2[4 * r4 + 2], z); z = fmaf(av[3], w2[4 * r4 + 3], z); }
;         const float la = (fminf(z, 0.f) - __logf(1.0f + __expf(-fabsf(z)))) * 0.0625f; run += la; bl[ii] = run; }
	v_fmac_f32_e32 v14, v8, v53
	v_fmac_f32_e32 v14, v9, v54
	v_fmac_f32_e32 v14, v10, v60
	v_fmac_f32_e32 v14, v11, v62
	v_mul_f32_e64 v4, |v14|, s3
	v_exp_f32_e32 v4, v4
	v_fmac_f32_e32 v13, 0x3377d1cf, v12
	v_fmac_f32_e32 v13, 0x3f317217, v12
	v_cmp_lt_f32_e64 s[34:35], |v12|, s43
	v_add_f32_e32 v4, 1.0, v4
	v_cndmask_b32_e32 v6, 0, v191, vcc
	v_cndmask_b32_e64 v5, v12, v13, s[34:35]
	v_cmp_gt_f32_e32 vcc, s31, v4
	v_sub_f32_e32 v5, v5, v6
	v_sub_f32_e32 v3, v3, v5
	v_cndmask_b32_e64 v6, 0, 32, vcc
	v_ldexp_f32 v4, v4, v6
	v_log_f32_e32 v12, v4
	ds_read_b128 v[4:7], v64 offset:320
	v_min_f32_e32 v13, 0, v14
	v_fmamk_f32 v3, v3, 0x3d800000, v1
	v_mul_f32_e32 v8, 0x3f317217, v12
	v_fma_f32 v14, v12, s42, -v8
	ds_read_b128 v[8:11], v64 offset:336
	s_waitcnt lgkmcnt(1)
	v_fma_f32 v15, v4, v55, v61
	v_fmac_f32_e32 v15, v5, v56
	v_fmac_f32_e32 v15, v6, v46
	v_fmac_f32_e32 v15, v7, v57
	ds_read_b128 v[4:7], v64 offset:352
	s_waitcnt lgkmcnt(1)
	v_fmac_f32_e32 v15, v8, v47
	v_fmac_f32_e32 v15, v9, v48
	v_fmac_f32_e32 v15, v10, v49
	v_fmac_f32_e32 v15, v11, v58
	ds_read_b128 v[8:11], v64 offset:368
	s_waitcnt lgkmcnt(1)
	v_fmac_f32_e32 v15, v4, v50
	v_fmac_f32_e32 v15, v5, v51
	v_fmac_f32_e32 v15, v6, v52
	v_fmac_f32_e32 v15, v7, v59
	s_waitcnt lgkmcnt(0)
	v_fmac_f32_e32 v15, v8, v53
	v_fmac_f32_e32 v15, v9, v54
	v_fmac_f32_e32 v15, v10, v60
	v_fmac_f32_e32 v15, v11, v62
	v_mul_f32_e64 v4, |v15|, s3
	v_exp_f32_e32 v4, v4
	v_fmac_f32_e32 v14, 0x3377d1cf, v12
	v_fmac_f32_e32 v14, 0x3f317217, v12
	v_cmp_lt_f32_e64 s[34:35], |v12|, s43
	v_add_f32_e32 v4, 1.0, v4
	v_cndmask_b32_e32 v6, 0, v191, vcc
	v_cndmask_b32_e64 v5, v12, v14, s[34:35]
	v_cmp_gt_f32_e32 vcc, s31, v4
	v_sub_f32_e32 v5, v5, v6
	v_sub_f32_e32 v5, v13, v5
	v_cndmask_b32_e64 v6, 0, 32, vcc
	v_ldexp_f32 v4, v4, v6
	v_log_f32_e32 v4, v4
	ds_read_b128 v[6:9], v64 offset:384
	v_min_f32_e32 v14, 0, v15
	v_fmamk_f32 v5, v5, 0x3d800000, v3
	v_mul_f32_e32 v10, 0x3f317217, v4
	v_fma_f32 v15, v4, s42, -v10
	ds_read_b128 v[10:13], v64 offset:400
	s_waitcnt lgkmcnt(1)
	v_fma_f32 v44, v6, v55, v61
	v_fmac_f32_e32 v44, v7, v56
	v_fmac_f32_e32 v44, v8, v46
	v_fmac_f32_e32 v44, v9, v57
	ds_read_b128 v[6:9], v64 offset:416
	s_waitcnt lgkmcnt(1)
	v_fmac_f32_e32 v44, v10, v47
	v_fmac_f32_e32 v44, v11, v48
	v_fmac_f32_e32 v44, v12, v49
	v_fmac_f32_e32 v44, v13, v58
	ds_read_b128 v[10:13], v64 offset:432
	s_waitcnt lgkmcnt(1)
	v_fmac_f32_e32 v44, v6, v50
	v_fmac_f32_e32 v44, v7, v51
	v_fmac_f32_e32 v44, v8, v52
	v_fmac_f32_e32 v44, v9, v59
	s_waitcnt lgkmcnt(0)
	v_fmac_f32_e32 v44, v10, v53
	v_fmac_f32_e32 v44, v11, v54
	v_fmac_f32_e32 v44, v12, v60
	v_fmac_f32_e32 v44, v13, v62
	v_mul_f32_e64 v6, |v44|, s3
	v_exp_f32_e32 v6, v6
	v_fmac_f32_e32 v15, 0x3377d1cf, v4
	v_fmac_f32_e32 v15, 0x3f317217, v4
	v_cmp_lt_f32_e64 s[34:35], |v4|, s43
	v_add_f32_e32 v6, 1.0, v6
	v_cndmask_b32_e32 v7, 0, v191, vcc
	v_cndmask_b32_e64 v4, v4, v15, s[34:35]
	v_cmp_gt_f32_e32 vcc, s31, v6
	v_sub_f32_e32 v4, v4, v7
	ds_read_b128 v[8:11], v64 offset:448
	v_cndmask_b32_e64 v7, 0, 32, vcc
	v_ldexp_f32 v6, v6, v7
	v_log_f32_e32 v7, v6
	v_sub_f32_e32 v4, v14, v4
	v_fmamk_f32 v6, v4, 0x3d800000, v5
	v_min_f32_e32 v4, 0, v44
	v_mul_f32_e32 v12, 0x3f317217, v7
	v_fma_f32 v44, v7, s42, -v12
	ds_read_b128 v[12:15], v64 offset:464
	s_waitcnt lgkmcnt(1)
	v_fma_f32 v45, v8, v55, v61
	v_fmac_f32_e32 v45, v9, v56
	v_fmac_f32_e32 v45, v10, v46
	v_fmac_f32_e32 v45, v11, v57
	ds_read_b128 v[8:11], v64 offset:480
	s_waitcnt lgkmcnt(1)
	v_fmac_f32_e32 v45, v12, v47
	v_fmac_f32_e32 v45, v13, v48
	v_fmac_f32_e32 v45, v14, v49
	v_fmac_f32_e32 v45, v15, v58
	ds_read_b128 v[12:15], v64 offset:496
	s_waitcnt lgkmcnt(1)
	v_fmac_f32_e32 v45, v8, v50
	v_fmac_f32_e32 v45, v9, v51
	v_fmac_f32_e32 v45, v10, v52
	v_fmac_f32_e32 v45, v11, v59
	s_waitcnt lgkmcnt(0)
	v_fmac_f32_e32 v45, v12, v53
	v_fmac_f32_e32 v45, v13, v54
	v_fmac_f32_e32 v45, v14, v60
	v_fmac_f32_e32 v45, v15, v62
	v_mul_f32_e64 v8, |v45|, s3
	v_exp_f32_e32 v8, v8
	v_fmac_f32_e32 v44, 0x3377d1cf, v7
	v_fmac_f32_e32 v44, 0x3f317217, v7
	v_cmp_lt_f32_e64 s[34:35], |v7|, s43
	v_add_f32_e32 v8, 1.0, v8
	v_cndmask_b32_e32 v9, 0, v191, vcc
	v_cndmask_b32_e64 v7, v7, v44, s[34:35]
	v_cmp_gt_f32_e32 vcc, s31, v8
	v_sub_f32_e32 v7, v7, v9
	v_sub_f32_e32 v4, v4, v7
	v_cndmask_b32_e64 v9, 0, 32, vcc
	v_ldexp_f32 v8, v8, v9
	v_log_f32_e32 v44, v8
	ds_read_b128 v[8:11], v64 offset:512
	v_fmamk_f32 v7, v4, 0x3d800000, v6
	v_min_f32_e32 v4, 0, v45
	v_mul_f32_e32 v12, 0x3f317217, v44
	v_fma_f32 v45, v44, s42, -v12
	ds_read_b128 v[12:15], v64 offset:528
	s_waitcnt lgkmcnt(1)
	v_fma_f32 v91, v8, v55, v61
	v_fmac_f32_e32 v91, v9, v56
	v_fmac_f32_e32 v91, v10, v46
	v_fmac_f32_e32 v91, v11, v57
	ds_read_b128 v[8:11], v64 offset:544
	s_waitcnt lgkmcnt(1)
	v_fmac_f32_e32 v91, v12, v47
	v_fmac_f32_e32 v91, v13, v48
	v_fmac_f32_e32 v91, v14, v49
	v_fmac_f32_e32 v91, v15, v58
	ds_read_b128 v[12:15], v64 offset:560
	s_waitcnt lgkmcnt(1)
	v_fmac_f32_e32 v91, v8, v50
	v_fmac_f32_e32 v91, v9, v51
	v_fmac_f32_e32 v91, v10, v52
	v_fmac_f32_e32 v91, v11, v59
	s_waitcnt lgkmcnt(0)
	v_fmac_f32_e32 v91, v12, v53
	v_fmac_f32_e32 v91, v13, v54
	v_fmac_f32_e32 v91, v14, v60
	v_fmac_f32_e32 v91, v15, v62
	ds_read_b128 v[12:15], v64 offset:576
	v_fmac_f32_e32 v45, 0x3377d1cf, v44
	v_fmac_f32_e32 v45, 0x3f317217, v44
	v_cmp_lt_f32_e64 s[34:35], |v44|, s43
	v_mul_f32_e64 v8, |v91|, s3
	v_exp_f32_e32 v8, v8
	v_cndmask_b32_e64 v9, v44, v45, s[34:35]
	s_waitcnt lgkmcnt(0)
; #define LAS __attribute__((address_space(3)))
; __device__ __forceinline__ void gla_local_unit(LAS unsigned char* lds, GlaPre& R, const bf16_t* proj, const float* alow, const float (&w2)[16], const float bias, ...
;     ...
;     for (int ii = 0; ii < 16; ++ii) { float z = bias; const LAS f32x4* ap = (const LAS f32x4*)(ALs + (16 * ig + ii) * 16);
; #pragma unroll
;         for (int r4 = 0; r4 < 4; ++r4) { const f32x4 av = ap[r4]; z = fmaf(av[0], w2[4 * r4], z); z = fmaf(av[1], w2[4 * r4 + 1], z); z = fmaf(av[2], w2[4 * r4 + 2], z); z = fmaf(av[3], w2[4 * r4 + 3], z); }
;         const float la = (fminf(z, 0.f) - __logf(1.0f + __expf(-fabsf(z)))) * 0.0625f; run += la; bl[ii] = run; }
	v_fma_f32 v44, v12, v55, v61
	v_fmac_f32_e32 v44, v13, v56
	v_fmac_f32_e32 v44, v14, v46
	v_fmac_f32_e32 v44, v15, v57
	ds_read_b128 v[12:15], v64 offset:608
	v_fmac_f32_e32 v44, v92, v47
	v_fmac_f32_e32 v44, v93, v48
	v_fmac_f32_e32 v44, v94, v49
	v_fmac_f32_e32 v44, v95, v58
	ds_read_b128 v[92:95], v64 offset:624
	v_add_f32_e32 v8, 1.0, v8
	s_waitcnt lgkmcnt(1)
	v_fmac_f32_e32 v44, v12, v50
	v_cndmask_b32_e32 v10, 0, v191, vcc
	v_cmp_gt_f32_e32 vcc, s31, v8
	v_fmac_f32_e32 v44, v13, v51
	v_sub_f32_e32 v9, v9, v10
	v_cndmask_b32_e64 v10, 0, 32, vcc
	v_fmac_f32_e32 v44, v14, v52
	v_ldexp_f32 v8, v8, v10
	v_fmac_f32_e32 v44, v15, v59
	v_log_f32_e32 v8, v8
	s_waitcnt lgkmcnt(0)
	v_fmac_f32_e32 v44, v92, v53
	v_fmac_f32_e32 v44, v93, v54
	v_fmac_f32_e32 v44, v94, v60
	v_fmac_f32_e32 v44, v95, v62
	v_sub_f32_e32 v4, v4, v9
	v_mul_f32_e32 v9, 0x3f317217, v8
	v_mul_f32_e64 v11, |v44|, s3
	v_fma_f32 v9, v8, s42, -v9
	v_exp_f32_e32 v11, v11
	v_fmac_f32_e32 v9, 0x3377d1cf, v8
	v_fmac_f32_e32 v9, 0x3f317217, v8
	v_cmp_lt_f32_e64 s[34:35], |v8|, s43
	ds_read_b128 v[12:15], v64 offset:640
	ds_read_b128 v[92:95], v64 offset:656
	v_cndmask_b32_e64 v8, v8, v9, s[34:35]
	v_cndmask_b32_e32 v9, 0, v191, vcc
	v_sub_f32_e32 v8, v8, v9
	v_add_f32_e32 v9, 1.0, v11
	v_fmamk_f32 v10, v4, 0x3d800000, v7
	v_min_f32_e32 v4, 0, v91
	v_cmp_gt_f32_e32 vcc, s31, v9
	v_sub_f32_e32 v4, v4, v8
	s_nop 0
	v_cndmask_b32_e64 v11, 0, 32, vcc
	v_ldexp_f32 v9, v9, v11
	v_fmamk_f32 v11, v4, 0x3d800000, v10
	v_min_f32_e32 v4, 0, v44
	s_waitcnt lgkmcnt(1)
	v_fma_f32 v44, v12, v55, v61
	v_fmac_f32_e32 v44, v13, v56
	v_fmac_f32_e32 v44, v14, v46
	v_fmac_f32_e32 v44, v15, v57
	ds_read_b128 v[12:15], v64 offset:672
	s_waitcnt lgkmcnt(1)
	v_fmac_f32_e32 v44, v92, v47
	v_fmac_f32_e32 v44, v93, v48
	v_fmac_f32_e32 v44, v94, v49
	v_fmac_f32_e32 v44, v95, v58
	ds_read_b128 v[92:95], v64 offset:688
	s_waitcnt lgkmcnt(1)
	v_fmac_f32_e32 v44, v12, v50
	v_fmac_f32_e32 v44, v13, v51
	v_fmac_f32_e32 v44, v14, v52
	v_fmac_f32_e32 v44, v15, v59
	v_log_f32_e32 v9, v9
	s_waitcnt lgkmcnt(0)
	v_fmac_f32_e32 v44, v92, v53
	v_fmac_f32_e32 v44, v93, v54
	v_fmac_f32_e32 v44, v94, v60
	v_fmac_f32_e32 v44, v95, v62
	v_mul_f32_e32 v8, 0x3f317217, v9
	v_mul_f32_e64 v12, |v44|, s3
	v_fma_f32 v8, v9, s42, -v8
	v_exp_f32_e32 v12, v12
	v_fmac_f32_e32 v8, 0x3377d1cf, v9
	v_fmac_f32_e32 v8, 0x3f317217, v9
	v_cmp_lt_f32_e64 s[34:35], |v9|, s43
	ds_read_b128 v[92:95], v64 offset:720
	s_nop 0
	v_cndmask_b32_e64 v8, v9, v8, s[34:35]
	v_cndmask_b32_e32 v9, 0, v191, vcc
	v_sub_f32_e32 v8, v8, v9
	v_add_f32_e32 v9, 1.0, v12
	v_cmp_gt_f32_e32 vcc, s31, v9
	v_sub_f32_e32 v4, v4, v8
	v_fmamk_f32 v8, v4, 0x3d800000, v11
	v_cndmask_b32_e64 v12, 0, 32, vcc
	v_ldexp_f32 v9, v9, v12
	ds_read_b128 v[12:15], v64 offset:704
	v_log_f32_e32 v9, v9
	v_min_f32_e32 v4, 0, v44
	s_waitcnt lgkmcnt(0)
	v_fma_f32 v45, v12, v55, v61
	v_fmac_f32_e32 v45, v13, v56
	v_fmac_f32_e32 v45, v14, v46
	v_fmac_f32_e32 v45, v15, v57
	ds_read_b128 v[12:15], v64 offset:736
	v_fmac_f32_e32 v45, v92, v47
	v_fmac_f32_e32 v45, v93, v48
	v_fmac_f32_e32 v45, v94, v49
	v_fmac_f32_e32 v45, v95, v58
	ds_read_b128 v[92:95], v64 offset:752
	s_waitcnt lgkmcnt(1)
	v_fmac_f32_e32 v45, v12, v50
	v_fmac_f32_e32 v45, v13, v51
	v_fmac_f32_e32 v45, v14, v52
	v_fmac_f32_e32 v45, v15, v59
	s_waitcnt lgkmcnt(0)
	v_fmac_f32_e32 v45, v92, v53
	v_fmac_f32_e32 v45, v93, v54
	v_fmac_f32_e32 v45, v94, v60
	v_fmac_f32_e32 v45, v95, v62
	v_mul_f32_e64 v12, |v45|, s3
	v_exp_f32_e32 v12, v12
	v_mul_f32_e32 v44, 0x3f317217, v9
	v_fma_f32 v44, v9, s42, -v44
	v_fmac_f32_e32 v44, 0x3377d1cf, v9
	v_fmac_f32_e32 v44, 0x3f317217, v9
	v_cmp_lt_f32_e64 s[34:35], |v9|, s43
	v_add_f32_e32 v12, 1.0, v12
	v_cndmask_b32_e32 v13, 0, v191, vcc
	v_cndmask_b32_e64 v9, v9, v44, s[34:35]
	v_cmp_gt_f32_e32 vcc, s31, v12
	v_sub_f32_e32 v9, v9, v13
	ds_read_b128 v[92:95], v64 offset:784
	v_cndmask_b32_e64 v13, 0, 32, vcc
	v_ldexp_f32 v12, v12, v13
	v_log_f32_e32 v44, v12
	ds_read_b128 v[12:15], v64 offset:768
	v_sub_f32_e32 v4, v4, v9
	v_fmamk_f32 v9, v4, 0x3d800000, v8
	v_min_f32_e32 v4, 0, v45
	v_mul_f32_e32 v45, 0x3f317217, v44
	s_waitcnt lgkmcnt(0)
	v_fma_f32 v91, v12, v55, v61
	v_fmac_f32_e32 v91, v13, v56
	v_fmac_f32_e32 v91, v14, v46
	v_fmac_f32_e32 v91, v15, v57
	ds_read_b128 v[12:15], v64 offset:800
	v_fmac_f32_e32 v91, v92, v47
	v_fmac_f32_e32 v91, v93, v48
	v_fmac_f32_e32 v91, v94, v49
	v_fmac_f32_e32 v91, v95, v58
	ds_read_b128 v[92:95], v64 offset:816
	s_waitcnt lgkmcnt(1)
	v_fmac_f32_e32 v91, v12, v50
	v_fmac_f32_e32 v91, v13, v51
	v_fmac_f32_e32 v91, v14, v52
	v_fmac_f32_e32 v91, v15, v59
	s_waitcnt lgkmcnt(0)
	v_fmac_f32_e32 v91, v92, v53
	v_fmac_f32_e32 v91, v93, v54
	v_fmac_f32_e32 v91, v94, v60
	v_fmac_f32_e32 v91, v95, v62
	ds_read_b128 v[92:95], v64 offset:832
	v_mul_f32_e64 v12, |v91|, s3
	v_exp_f32_e32 v12, v12
	v_fma_f32 v45, v44, s42, -v45
	v_fmac_f32_e32 v45, 0x3377d1cf, v44
	s_waitcnt lgkmcnt(0)
	v_fma_f32 v15, v92, v55, v61
	v_fmac_f32_e32 v15, v93, v56
	v_fmac_f32_e32 v15, v94, v46
	v_fmac_f32_e32 v15, v95, v57
	ds_read_b128 v[92:95], v64 offset:864
	v_fmac_f32_e32 v15, v96, v47
	v_fmac_f32_e32 v15, v97, v48
	v_fmac_f32_e32 v15, v98, v49
	v_fmac_f32_e32 v15, v99, v58
	ds_read_b128 v[96:99], v64 offset:880
	v_fmac_f32_e32 v45, 0x3f317217, v44
	v_cmp_lt_f32_e64 s[34:35], |v44|, s43
	v_add_f32_e32 v12, 1.0, v12
	s_waitcnt lgkmcnt(1)
	v_fmac_f32_e32 v15, v92, v50
	v_cndmask_b32_e64 v13, v44, v45, s[34:35]
	v_cndmask_b32_e32 v14, 0, v191, vcc
	v_cmp_gt_f32_e32 vcc, s31, v12
	v_fmac_f32_e32 v15, v93, v51
	v_sub_f32_e32 v13, v13, v14
	v_cndmask_b32_e64 v14, 0, 32, vcc
	v_fmac_f32_e32 v15, v94, v52
	v_ldexp_f32 v12, v12, v14
	v_fmac_f32_e32 v15, v95, v59
	v_log_f32_e32 v14, v12
	s_waitcnt lgkmcnt(0)
; #define LAS __attribute__((address_space(3)))
; __device__ __forceinline__ unsigned f2bf(float f) { unsigned u = __builtin_bit_cast(unsigned, f); return (u + 0x7fffu + ((u >> 16) & 1u)) >> 16; }
; __device__ __forceinline__ void gla_local_unit(LAS unsigned char* lds, GlaPre& R, const bf16_t* proj, const float* alow, const float (&w2)[16], const float bias, ...
;     ...
;     for (int ii = 0; ii < 16; ++ii) { float z = bias; const LAS f32x4* ap = (const LAS f32x4*)(ALs + (16 * ig + ii) * 16);
; #pragma unroll
;         for (int r4 = 0; r4 < 4; ++r4) { const f32x4 av = ap[r4]; z = fmaf(av[0], w2[4 * r4], z); z = fmaf(av[1], w2[4 * r4 + 1], z); z = fmaf(av[2], w2[4 * r4 + 2], z); z = fmaf(av[3], w2[4 * r4 + 3], z); }
;         const float la = (fminf(z, 0.f) - __logf(1.0f + __expf(-fabsf(z)))) * 0.0625f; run += la; bl[ii] = run; }
;     CS[ig * 128 + d] = run;
;     __syncthreads();
;     float pre = 0.f, tot = 0.f;
; #pragma unroll
;     for (int g2 = 0; g2 < 4; ++g2) { const float cv = CS[g2 * 128 + d]; tot += cv; pre += (g2 < ig) ? cv : 0.f; }
;     const float qscale = 0.08838834764831845f; const float etot = __expf(tot);
;     unsigned ke[8];
; #pragma unroll
;     for (int ii = 0; ii < 16; ++ii) { const float bb = pre + bl[ii];
;         LAS bf16_t* qp = (LAS bf16_t*)(QD + (16 * ig + ii) * 272 + 2 * d); LAS bf16_t* kp = (LAS bf16_t*)(KI + (16 * ig + ii) * 272 + 2 * d);
;         const float qf_ = bf2f(*qp), kf_ = bf2f(*kp);
;         const float eb = __expf(bb), einv = __builtin_amdgcn_rcpf(eb);
;         const float qd = qf_ * qscale * eb, ki = kf_ * einv, kend = kf_ * (etot * einv);
;         *qp = (bf16_t)f2bf(qd); *kp = (bf16_t)f2bf(ki);
;         if (ii & 1) ke[ii >> 1] |= f2bf(kend) << 16; else ke[ii >> 1] = f2bf(kend); }
	v_fmac_f32_e32 v15, v96, v53
	v_fmac_f32_e32 v15, v97, v54
	v_fmac_f32_e32 v15, v98, v60
	v_fmac_f32_e32 v15, v99, v62
	v_sub_f32_e32 v4, v4, v13
	v_mul_f32_e32 v13, 0x3f317217, v14
	v_mul_f32_e64 v44, |v15|, s3
	v_fma_f32 v13, v14, s42, -v13
	v_exp_f32_e32 v44, v44
	v_fmac_f32_e32 v13, 0x3377d1cf, v14
	v_fmac_f32_e32 v13, 0x3f317217, v14
	v_cmp_lt_f32_e64 s[34:35], |v14|, s43
	ds_read_b128 v[92:95], v64 offset:896
	ds_read_b128 v[96:99], v64 offset:912
	v_cndmask_b32_e64 v13, v14, v13, s[34:35]
	v_cndmask_b32_e32 v14, 0, v191, vcc
	v_sub_f32_e32 v13, v13, v14
	v_add_f32_e32 v14, 1.0, v44
	v_cmp_gt_f32_e32 vcc, s31, v14
	v_fmamk_f32 v12, v4, 0x3d800000, v9
	v_min_f32_e32 v4, 0, v91
	v_cndmask_b32_e64 v44, 0, 32, vcc
	v_ldexp_f32 v14, v14, v44
	s_waitcnt lgkmcnt(1)
	v_fma_f32 v44, v92, v55, v61
	v_fmac_f32_e32 v44, v93, v56
	v_fmac_f32_e32 v44, v94, v46
	v_fmac_f32_e32 v44, v95, v57
	ds_read_b128 v[92:95], v64 offset:928
	s_waitcnt lgkmcnt(1)
	v_fmac_f32_e32 v44, v96, v47
	v_fmac_f32_e32 v44, v97, v48
	v_fmac_f32_e32 v44, v98, v49
	v_fmac_f32_e32 v44, v99, v58
	ds_read_b128 v[96:99], v64 offset:944
	s_waitcnt lgkmcnt(1)
	v_fmac_f32_e32 v44, v92, v50
	v_fmac_f32_e32 v44, v93, v51
	v_fmac_f32_e32 v44, v94, v52
	v_fmac_f32_e32 v44, v95, v59
	v_log_f32_e32 v14, v14
	s_waitcnt lgkmcnt(0)
	v_fmac_f32_e32 v44, v96, v53
	v_fmac_f32_e32 v44, v97, v54
	v_fmac_f32_e32 v44, v98, v60
	v_sub_f32_e32 v4, v4, v13
	v_fmac_f32_e32 v44, v99, v62
	v_fmamk_f32 v13, v4, 0x3d800000, v12
	v_min_f32_e32 v4, 0, v15
	v_mul_f32_e32 v15, 0x3f317217, v14
	v_mul_f32_e64 v45, |v44|, s3
	v_fma_f32 v15, v14, s42, -v15
	v_exp_f32_e32 v45, v45
	v_fmac_f32_e32 v15, 0x3377d1cf, v14
	v_fmac_f32_e32 v15, 0x3f317217, v14
	v_cmp_lt_f32_e64 s[34:35], |v14|, s43
	ds_read_b128 v[92:95], v64 offset:960
	ds_read_b128 v[96:99], v64 offset:976
	v_cndmask_b32_e64 v14, v14, v15, s[34:35]
	v_cndmask_b32_e32 v15, 0, v191, vcc
	v_sub_f32_e32 v14, v14, v15
	v_add_f32_e32 v15, 1.0, v45
	v_cmp_gt_f32_e32 vcc, s31, v15
	v_sub_f32_e32 v4, v4, v14
	v_fmamk_f32 v14, v4, 0x3d800000, v13
	v_cndmask_b32_e64 v45, 0, 32, vcc
	v_ldexp_f32 v15, v15, v45
	s_waitcnt lgkmcnt(1)
	v_fma_f32 v45, v92, v55, v61
	v_fmac_f32_e32 v45, v93, v56
	v_fmac_f32_e32 v45, v94, v46
	v_fmac_f32_e32 v45, v95, v57
	ds_read_b128 v[92:95], v64 offset:992
	s_waitcnt lgkmcnt(1)
	v_fmac_f32_e32 v45, v96, v47
	v_fmac_f32_e32 v45, v97, v48
	v_fmac_f32_e32 v45, v98, v49
	v_fmac_f32_e32 v45, v99, v58
	ds_read_b128 v[96:99], v64 offset:1008
	s_waitcnt lgkmcnt(1)
	v_fmac_f32_e32 v45, v92, v50
	v_fmac_f32_e32 v45, v93, v51
	v_fmac_f32_e32 v45, v94, v52
	v_fmac_f32_e32 v45, v95, v59
	v_log_f32_e32 v15, v15
	s_waitcnt lgkmcnt(0)
	v_fmac_f32_e32 v45, v96, v53
	v_fmac_f32_e32 v45, v97, v54
	v_fmac_f32_e32 v45, v98, v60
	v_fmac_f32_e32 v45, v99, v62
	v_min_f32_e32 v4, 0, v44
	v_mul_f32_e32 v44, 0x3f317217, v15
	v_mul_f32_e64 v91, |v45|, s3
	v_fma_f32 v44, v15, s42, -v44
	v_exp_f32_e32 v91, v91
	v_fmac_f32_e32 v44, 0x3377d1cf, v15
	v_fmac_f32_e32 v44, 0x3f317217, v15
	v_cmp_lt_f32_e64 s[34:35], |v15|, s43
	s_nop 1
	v_cndmask_b32_e64 v15, v15, v44, s[34:35]
	v_cndmask_b32_e32 v44, 0, v191, vcc
	v_sub_f32_e32 v15, v15, v44
	v_add_f32_e32 v44, 1.0, v91
	v_cmp_gt_f32_e32 vcc, s31, v44
	v_sub_f32_e32 v4, v4, v15
	v_fmamk_f32 v15, v4, 0x3d800000, v14
	v_cndmask_b32_e64 v91, 0, 32, vcc
	v_ldexp_f32 v44, v44, v91
	v_log_f32_e32 v44, v44
	v_min_f32_e32 v4, 0, v45
	v_mul_f32_e32 v45, 0x3f317217, v44
	v_fma_f32 v45, v44, s42, -v45
	v_fmac_f32_e32 v45, 0x3377d1cf, v44
	v_fmac_f32_e32 v45, 0x3f317217, v44
	v_cmp_lt_f32_e64 s[34:35], |v44|, s43
	s_nop 1
	v_cndmask_b32_e64 v44, v44, v45, s[34:35]
	v_cndmask_b32_e32 v45, 0, v191, vcc
	v_sub_f32_e32 v44, v44, v45
	v_sub_f32_e32 v4, v4, v44
	v_fmamk_f32 v44, v4, 0x3d800000, v15
	ds_write_b32 v65, v44
	s_waitcnt lgkmcnt(0)
	s_barrier
	ds_read2st64_b32 v[92:93], v66 offset1:2
	ds_read2st64_b32 v[94:95], v66 offset0:4 offset1:6
	s_waitcnt lgkmcnt(1)
	v_add_f32_e32 v4, 0, v92
	v_cndmask_b32_e64 v45, 0, v4, s[4:5]
	v_cndmask_b32_e64 v91, 0, v93, s[6:7]
	v_add_f32_e32 v45, v45, v91
	s_waitcnt lgkmcnt(0)
	v_cndmask_b32_e64 v91, 0, v94, s[8:9]
	v_add_f32_e32 v45, v45, v91
	v_cndmask_b32_e64 v91, 0, v95, s[10:11]
	v_add_f32_e32 v45, v45, v91
	v_add_f32_e32 v2, v2, v45
	v_mul_f32_e32 v2, 0x3fb8aa3b, v2
	v_exp_f32_e32 v2, v2
	ds_read_u16 v91, v77
	ds_read_u16 v92, v77 offset:272
	ds_read_u16 v96, v77 offset:544
	ds_read_u16 v97, v77 offset:816
	ds_read_u16 v98, v77 offset:1088
	ds_read_u16 v99, v77 offset:1360
	ds_read_u16 v100, v77 offset:1632
	ds_read_u16 v101, v77 offset:1904
	s_waitcnt lgkmcnt(7)
	v_lshlrev_b32_e32 v91, 16, v91
	v_mul_f32_e32 v91, 0x3db504f3, v91
	v_add_f32_e32 v4, v4, v93
	v_rcp_f32_e32 v93, v2
	v_mul_f32_e32 v2, v2, v91
	v_bfe_u32 v91, v2, 16, 1
	v_add_f32_e32 v0, v0, v45
	v_mul_f32_e32 v0, 0x3fb8aa3b, v0
	v_add3_u32 v2, v2, v91, s33
	v_exp_f32_e32 v0, v0
	ds_write_b16_d16_hi v77, v2
	v_add_f32_e32 v4, v4, v94
	ds_read_u16 v91, v77 offset:17680
	ds_read_u16 v102, v77 offset:18224
	ds_read_u16 v103, v77 offset:18496
	ds_read_u16 v104, v77 offset:18768
	ds_read_u16 v105, v77 offset:19040
	ds_read_u16 v106, v77 offset:19312
	ds_read_u16 v107, v77 offset:17952
	ds_read_u16 v94, v77 offset:17408
	s_waitcnt lgkmcnt(14)
	v_lshlrev_b32_e32 v2, 16, v92
	v_mul_f32_e32 v2, 0x3db504f3, v2
	v_rcp_f32_e32 v92, v0
	v_mul_f32_e32 v0, v0, v2
	v_add_f32_e32 v4, v4, v95
	v_bfe_u32 v2, v0, 16, 1
	v_mul_f32_e32 v4, 0x3fb8aa3b, v4
	v_add3_u32 v0, v0, v2, s33
	s_waitcnt lgkmcnt(0)
; #define LAS __attribute__((address_space(3)))
; __device__ __forceinline__ unsigned f2bf(float f) { unsigned u = __builtin_bit_cast(unsigned, f); return (u + 0x7fffu + ((u >> 16) & 1u)) >> 16; }
; __device__ __forceinline__ void gla_local_unit(LAS unsigned char* lds, GlaPre& R, const bf16_t* proj, const float* alow, const float (&w2)[16], const float bias, ...
;     ...
;     for (int ii = 0; ii < 16; ++ii) { const float bb = pre + bl[ii];
;         LAS bf16_t* qp = (LAS bf16_t*)(QD + (16 * ig + ii) * 272 + 2 * d); LAS bf16_t* kp = (LAS bf16_t*)(KI + (16 * ig + ii) * 272 + 2 * d);
;         const float qf_ = bf2f(*qp), kf_ = bf2f(*kp);
;         const float eb = __expf(bb), einv = __builtin_amdgcn_rcpf(eb);
;         const float qd = qf_ * qscale * eb, ki = kf_ * einv, kend = kf_ * (etot * einv);
;         *qp = (bf16_t)f2bf(qd); *kp = (bf16_t)f2bf(ki);
;         if (ii & 1) ke[ii >> 1] |= f2bf(kend) << 16; else ke[ii >> 1] = f2bf(kend); }
	v_lshlrev_b32_e32 v95, 16, v94
	v_exp_f32_e32 v4, v4
	ds_write_b16_d16_hi v77, v0 offset:272
	v_mul_f32_e32 v0, v93, v95
	v_bfe_u32 v2, v0, 16, 1
	v_lshlrev_b32_e32 v94, 16, v91
	v_add3_u32 v0, v0, v2, s33
	ds_write_b16_d16_hi v77, v0 offset:17408
	v_mul_f32_e32 v0, v92, v94
	v_bfe_u32 v2, v0, 16, 1
	v_pk_mul_f32 v[92:93], v[4:5], v[92:93] op_sel_hi:[0,1]
	v_add3_u32 v0, v0, v2, s33
	v_pk_mul_f32 v[92:93], v[92:93], v[94:95]
	v_add_f32_e32 v1, v1, v45
	ds_write_b16_d16_hi v77, v0 offset:17680
	v_and_b32_sdwa v0, v93, v188 dst_sel:DWORD dst_unused:UNUSED_PAD src0_sel:WORD_1 src1_sel:DWORD
	v_mul_f32_e32 v1, 0x3fb8aa3b, v1
	v_and_b32_sdwa v2, v92, v188 dst_sel:DWORD dst_unused:UNUSED_PAD src0_sel:WORD_1 src1_sel:DWORD
	v_add3_u32 v0, v93, v0, s33
	v_exp_f32_e32 v1, v1
	v_add3_u32 v2, v92, v2, s33
	v_lshrrev_b32_e32 v0, 16, v0
	v_and_or_b32 v0, v2, s2, v0
	v_lshlrev_b32_e32 v2, 16, v96
	v_mul_f32_e32 v2, 0x3db504f3, v2
	v_add_f32_e32 v3, v3, v45
	v_rcp_f32_e32 v93, v1
	v_mul_f32_e32 v1, v1, v2
	v_mul_f32_e32 v3, 0x3fb8aa3b, v3
	v_bfe_u32 v2, v1, 16, 1
	v_exp_f32_e32 v3, v3
	v_add3_u32 v1, v1, v2, s33
	ds_write_b16_d16_hi v77, v1 offset:544
	v_lshlrev_b32_e32 v1, 16, v97
	v_mul_f32_e32 v1, 0x3db504f3, v1
	v_mul_f32_e32 v1, v3, v1
	v_bfe_u32 v2, v1, 16, 1
	v_rcp_f32_e32 v92, v3
	v_add3_u32 v1, v1, v2, s33
	v_lshlrev_b32_e32 v3, 16, v107
	ds_write_b16_d16_hi v77, v1 offset:816
	v_mul_f32_e32 v1, v93, v3
	v_bfe_u32 v91, v1, 16, 1
	v_lshlrev_b32_e32 v2, 16, v102
	v_add3_u32 v1, v1, v91, s33
	ds_write_b16_d16_hi v77, v1 offset:17952
	v_mul_f32_e32 v1, v92, v2
	v_bfe_u32 v91, v1, 16, 1
	v_pk_mul_f32 v[92:93], v[4:5], v[92:93] op_sel_hi:[0,1]
	v_add3_u32 v1, v1, v91, s33
	v_pk_mul_f32 v[2:3], v[92:93], v[2:3]
	ds_write_b16_d16_hi v77, v1 offset:18224
	v_and_b32_sdwa v1, v3, v188 dst_sel:DWORD dst_unused:UNUSED_PAD src0_sel:WORD_1 src1_sel:DWORD
	v_add3_u32 v1, v3, v1, s33
	v_add_f32_e32 v3, v5, v45
	v_mul_f32_e32 v3, 0x3fb8aa3b, v3
	v_and_b32_sdwa v91, v2, v188 dst_sel:DWORD dst_unused:UNUSED_PAD src0_sel:WORD_1 src1_sel:DWORD
	v_exp_f32_e32 v5, v3
	v_add3_u32 v2, v2, v91, s33
	v_lshrrev_b32_e32 v1, 16, v1
	v_and_or_b32 v1, v2, s2, v1
	v_lshlrev_b32_e32 v2, 16, v98
	v_add_f32_e32 v6, v6, v45
	v_mul_f32_e32 v2, 0x3db504f3, v2
	v_mul_f32_e32 v6, 0x3fb8aa3b, v6
	v_mul_f32_e32 v2, v5, v2
	v_exp_f32_e32 v6, v6
	v_rcp_f32_e32 v3, v5
	v_bfe_u32 v5, v2, 16, 1
	v_add3_u32 v2, v2, v5, s33
	v_lshlrev_b32_e32 v5, 16, v99
	v_mul_f32_e32 v5, 0x3db504f3, v5
	v_mul_f32_e32 v5, v6, v5
	ds_write_b16_d16_hi v77, v2 offset:1088
	v_rcp_f32_e32 v2, v6
	v_bfe_u32 v6, v5, 16, 1
	v_add3_u32 v5, v5, v6, s33
	v_lshlrev_b32_e32 v93, 16, v103
	ds_write_b16_d16_hi v77, v5 offset:1360
	v_mul_f32_e32 v5, v3, v93
	v_bfe_u32 v6, v5, 16, 1
	v_lshlrev_b32_e32 v92, 16, v104
	v_add3_u32 v5, v5, v6, s33
	ds_write_b16_d16_hi v77, v5 offset:18496
	v_mul_f32_e32 v5, v2, v92
	v_bfe_u32 v6, v5, 16, 1
	v_add3_u32 v5, v5, v6, s33
	v_pk_mul_f32 v[2:3], v[4:5], v[2:3] op_sel_hi:[0,1]
	v_pk_mul_f32 v[2:3], v[2:3], v[92:93]
	ds_write_b16_d16_hi v77, v5 offset:18768
	v_and_b32_sdwa v5, v3, v188 dst_sel:DWORD dst_unused:UNUSED_PAD src0_sel:WORD_1 src1_sel:DWORD
	v_add3_u32 v3, v3, v5, s33
	v_add_f32_e32 v5, v7, v45
	v_mul_f32_e32 v5, 0x3fb8aa3b, v5
	v_and_b32_sdwa v6, v2, v188 dst_sel:DWORD dst_unused:UNUSED_PAD src0_sel:WORD_1 src1_sel:DWORD
	v_exp_f32_e32 v5, v5
	v_add3_u32 v2, v2, v6, s33
	v_lshrrev_b32_e32 v3, 16, v3
	v_and_or_b32 v2, v2, s2, v3
	v_lshlrev_b32_e32 v3, 16, v100
	v_mul_f32_e32 v3, 0x3db504f3, v3
	v_add_f32_e32 v6, v10, v45
	v_mul_f32_e32 v3, v5, v3
	v_mul_f32_e32 v6, 0x3fb8aa3b, v6
	v_rcp_f32_e32 v7, v5
	v_bfe_u32 v5, v3, 16, 1
	v_exp_f32_e32 v10, v6
	v_add3_u32 v3, v3, v5, s33
	ds_write_b16_d16_hi v77, v3 offset:1632
	v_lshlrev_b32_e32 v3, 16, v101
	v_mul_f32_e32 v3, 0x3db504f3, v3
	v_mul_f32_e32 v3, v10, v3
	v_bfe_u32 v5, v3, 16, 1
	v_rcp_f32_e32 v6, v10
	v_add3_u32 v3, v3, v5, s33
	v_lshlrev_b32_e32 v93, 16, v105
	ds_write_b16_d16_hi v77, v3 offset:1904
	v_mul_f32_e32 v3, v7, v93
	v_bfe_u32 v5, v3, 16, 1
	v_lshlrev_b32_e32 v92, 16, v106
	v_add3_u32 v3, v3, v5, s33
	ds_write_b16_d16_hi v77, v3 offset:19040
	v_mul_f32_e32 v3, v6, v92
	v_bfe_u32 v5, v3, 16, 1
	v_pk_mul_f32 v[6:7], v[4:5], v[6:7] op_sel_hi:[0,1]
	v_add3_u32 v3, v3, v5, s33
	v_pk_mul_f32 v[6:7], v[6:7], v[92:93]
	ds_write_b16_d16_hi v77, v3 offset:19312
	v_and_b32_sdwa v3, v7, v188 dst_sel:DWORD dst_unused:UNUSED_PAD src0_sel:WORD_1 src1_sel:DWORD
	v_and_b32_sdwa v5, v6, v188 dst_sel:DWORD dst_unused:UNUSED_PAD src0_sel:WORD_1 src1_sel:DWORD
	v_add3_u32 v3, v7, v3, s33
	v_add3_u32 v5, v6, v5, s33
	v_lshrrev_b32_e32 v3, 16, v3
	v_and_or_b32 v3, v5, s2, v3
	v_add_f32_e32 v5, v11, v45
	v_mul_f32_e32 v5, 0x3fb8aa3b, v5
	v_exp_f32_e32 v5, v5
	ds_read_u16 v6, v77 offset:2176
	ds_read_u16 v10, v77 offset:2448
	ds_read_u16 v91, v77 offset:2720
	ds_read_u16 v92, v77 offset:2992
	ds_read_u16 v93, v77 offset:3264
	ds_read_u16 v94, v77 offset:3536
	ds_read_u16 v95, v77 offset:3808
	ds_read_u16 v96, v77 offset:4080
	s_waitcnt lgkmcnt(7)
	v_lshlrev_b32_e32 v6, 16, v6
	v_mul_f32_e32 v6, 0x3db504f3, v6
	v_add_f32_e32 v8, v8, v45
	v_rcp_f32_e32 v7, v5
	v_mul_f32_e32 v5, v5, v6
	v_mul_f32_e32 v8, 0x3fb8aa3b, v8
	v_bfe_u32 v6, v5, 16, 1
	v_exp_f32_e32 v8, v8
	v_add3_u32 v5, v5, v6, s33
	ds_write_b16_d16_hi v77, v5 offset:2176
	s_waitcnt lgkmcnt(7)
	v_lshlrev_b32_e32 v5, 16, v10
	v_mul_f32_e32 v5, 0x3db504f3, v5
	v_mul_f32_e32 v5, v8, v5
	v_rcp_f32_e32 v6, v8
	v_bfe_u32 v8, v5, 16, 1
	v_add3_u32 v5, v5, v8, s33
	ds_write_b16_d16_hi v77, v5 offset:2448
	ds_read_u16 v5, v77 offset:19584
	ds_read_u16 v8, v77 offset:19856
	ds_read_u16 v97, v77 offset:20128
	ds_read_u16 v98, v77 offset:20400
	ds_read_u16 v99, v77 offset:20672
	ds_read_u16 v100, v77 offset:20944
	ds_read_u16 v101, v77 offset:21216
	ds_read_u16 v102, v77 offset:21488
	s_waitcnt lgkmcnt(7)
; #define LAS __attribute__((address_space(3)))
; __device__ __forceinline__ unsigned f2bf(float f) { unsigned u = __builtin_bit_cast(unsigned, f); return (u + 0x7fffu + ((u >> 16) & 1u)) >> 16; }
; __device__ __forceinline__ void gla_local_unit(LAS unsigned char* lds, GlaPre& R, const bf16_t* proj, const float* alow, const float (&w2)[16], const float bias, ...
;     ...
;     for (int ii = 0; ii < 16; ++ii) { const float bb = pre + bl[ii];
;         LAS bf16_t* qp = (LAS bf16_t*)(QD + (16 * ig + ii) * 272 + 2 * d); LAS bf16_t* kp = (LAS bf16_t*)(KI + (16 * ig + ii) * 272 + 2 * d);
;         const float qf_ = bf2f(*qp), kf_ = bf2f(*kp);
;         const float eb = __expf(bb), einv = __builtin_amdgcn_rcpf(eb);
;         const float qd = qf_ * qscale * eb, ki = kf_ * einv, kend = kf_ * (etot * einv);
;         *qp = (bf16_t)f2bf(qd); *kp = (bf16_t)f2bf(ki);
;         if (ii & 1) ke[ii >> 1] |= f2bf(kend) << 16; else ke[ii >> 1] = f2bf(kend); }
;     *(LAS u32x4*)(KET + d * 144 + 32 * ig) = (u32x4){ke[0], ke[1], ke[2], ke[3]}; *(LAS u32x4*)(KET + d * 144 + 32 * ig + 16) = (u32x4){ke[4], ke[5], ke[6], ke[7]};
;     if (ig == 0) decg[(size_t)u * 128 + d] = etot;
;     __syncthreads();
; #pragma unroll
;     for (int it = 0; it < 2; ++it) { const int id = tid + NTHREADS * it, row = id >> 4, ch = id & 15; *(u32x4*)(qdg + ((size_t)(b * 4 + h) * 32 + n) * 8192 + (size_t)((((row >> 4) * 4 + (ch >> 2)) * 64 + (row & 15) * 4 + (ch & 3)) * 8)) = *(const LAS u32x4*)(QD + row * 272 + ch * 16); }
; #pragma unroll
;     for (int x = 0; x < 2; ++x) { const int id = 2 * wave + x, ti = id >> 2, tj = id & 3; f32x4 acc = (f32x4){0.f, 0.f, 0.f, 0.f};
;         if (tj <= ti) {
; #pragma unroll
;             for (int ks = 0; ks < 4; ++ks) { const bf16x8 af = *(const LAS bf16x8*)(QD + (16 * ti + fr) * 272 + (32 * ks + 8 * fq) * 2); const bf16x8 bfr = *(const LAS bf16x8*)(KI + (16 * tj + fr) * 272 + (32 * ks + 8 * fq) * 2);
;                 acc = __builtin_amdgcn_mfma_f32_16x16x32_bf16(af, bfr, acc, 0, 0, 0); } }
	v_lshlrev_b32_e32 v11, 16, v5
	v_mul_f32_e32 v5, v7, v11
	s_waitcnt lgkmcnt(6)
	v_lshlrev_b32_e32 v10, 16, v8
	v_bfe_u32 v8, v5, 16, 1
	v_add3_u32 v5, v5, v8, s33
	ds_write_b16_d16_hi v77, v5 offset:19584
	v_mul_f32_e32 v5, v6, v10
	v_bfe_u32 v8, v5, 16, 1
	v_add3_u32 v5, v5, v8, s33
	v_pk_mul_f32 v[6:7], v[4:5], v[6:7] op_sel_hi:[0,1]
	v_pk_mul_f32 v[6:7], v[6:7], v[10:11]
	ds_write_b16_d16_hi v77, v5 offset:19856
	v_and_b32_sdwa v5, v7, v188 dst_sel:DWORD dst_unused:UNUSED_PAD src0_sel:WORD_1 src1_sel:DWORD
	v_add3_u32 v5, v7, v5, s33
	v_add_f32_e32 v7, v9, v45
	v_mul_f32_e32 v7, 0x3fb8aa3b, v7
	v_and_b32_sdwa v8, v6, v188 dst_sel:DWORD dst_unused:UNUSED_PAD src0_sel:WORD_1 src1_sel:DWORD
	v_exp_f32_e32 v7, v7
	v_add3_u32 v6, v6, v8, s33
	v_lshrrev_b32_e32 v5, 16, v5
	v_and_or_b32 v6, v6, s2, v5
	v_lshlrev_b32_e32 v5, 16, v91
	v_mul_f32_e32 v5, 0x3db504f3, v5
	v_add_f32_e32 v8, v12, v45
	v_mul_f32_e32 v5, v7, v5
	v_mul_f32_e32 v8, 0x3fb8aa3b, v8
	v_rcp_f32_e32 v9, v7
	v_bfe_u32 v7, v5, 16, 1
	v_exp_f32_e32 v10, v8
	v_add3_u32 v5, v5, v7, s33
	ds_write_b16_d16_hi v77, v5 offset:2720
	v_lshlrev_b32_e32 v5, 16, v92
	v_mul_f32_e32 v5, 0x3db504f3, v5
	v_mul_f32_e32 v5, v10, v5
	v_bfe_u32 v7, v5, 16, 1
	v_rcp_f32_e32 v8, v10
	v_add3_u32 v5, v5, v7, s33
	s_waitcnt lgkmcnt(8)
	v_lshlrev_b32_e32 v11, 16, v97
	ds_write_b16_d16_hi v77, v5 offset:2992
	v_mul_f32_e32 v5, v9, v11
	v_bfe_u32 v7, v5, 16, 1
	s_waitcnt lgkmcnt(8)
	v_lshlrev_b32_e32 v10, 16, v98
	v_add3_u32 v5, v5, v7, s33
	ds_write_b16_d16_hi v77, v5 offset:20128
	v_mul_f32_e32 v5, v8, v10
	v_bfe_u32 v7, v5, 16, 1
	v_add3_u32 v5, v5, v7, s33
	v_pk_mul_f32 v[8:9], v[4:5], v[8:9] op_sel_hi:[0,1]
	v_pk_mul_f32 v[8:9], v[8:9], v[10:11]
	ds_write_b16_d16_hi v77, v5 offset:20400
	v_and_b32_sdwa v7, v8, v188 dst_sel:DWORD dst_unused:UNUSED_PAD src0_sel:WORD_1 src1_sel:DWORD
	v_add3_u32 v7, v8, v7, s33
	v_add_f32_e32 v8, v45, v13
	v_and_b32_sdwa v5, v9, v188 dst_sel:DWORD dst_unused:UNUSED_PAD src0_sel:WORD_1 src1_sel:DWORD
	v_mul_f32_e32 v8, 0x3fb8aa3b, v8
	v_add3_u32 v5, v9, v5, s33
	v_exp_f32_e32 v8, v8
	v_lshrrev_b32_e32 v5, 16, v5
	v_and_or_b32 v7, v7, s2, v5
	v_lshlrev_b32_e32 v5, 16, v93
	v_mul_f32_e32 v5, 0x3db504f3, v5
	v_add_f32_e32 v10, v45, v14
	v_mul_f32_e32 v5, v8, v5
	v_mul_f32_e32 v10, 0x3fb8aa3b, v10
	v_rcp_f32_e32 v9, v8
	v_bfe_u32 v8, v5, 16, 1
	v_exp_f32_e32 v10, v10
	v_add3_u32 v5, v5, v8, s33
	ds_write_b16_d16_hi v77, v5 offset:3264
	v_lshlrev_b32_e32 v5, 16, v94
	v_mul_f32_e32 v5, 0x3db504f3, v5
	v_mul_f32_e32 v5, v10, v5
	v_rcp_f32_e32 v8, v10
	v_bfe_u32 v10, v5, 16, 1
	v_add3_u32 v5, v5, v10, s33
	s_waitcnt lgkmcnt(10)
	v_lshlrev_b32_e32 v11, 16, v99
	ds_write_b16_d16_hi v77, v5 offset:3536
	v_mul_f32_e32 v5, v9, v11
	v_bfe_u32 v12, v5, 16, 1
	s_waitcnt lgkmcnt(10)
	v_lshlrev_b32_e32 v10, 16, v100
	v_add3_u32 v5, v5, v12, s33
	ds_write_b16_d16_hi v77, v5 offset:20672
	v_mul_f32_e32 v5, v8, v10
	v_bfe_u32 v12, v5, 16, 1
	v_add3_u32 v5, v5, v12, s33
	v_pk_mul_f32 v[8:9], v[4:5], v[8:9] op_sel_hi:[0,1]
	v_pk_mul_f32 v[8:9], v[8:9], v[10:11]
	ds_write_b16_d16_hi v77, v5 offset:20944
	v_and_b32_sdwa v5, v9, v188 dst_sel:DWORD dst_unused:UNUSED_PAD src0_sel:WORD_1 src1_sel:DWORD
	v_add3_u32 v5, v9, v5, s33
	v_add_f32_e32 v9, v45, v15
	v_mul_f32_e32 v9, 0x3fb8aa3b, v9
	v_and_b32_sdwa v10, v8, v188 dst_sel:DWORD dst_unused:UNUSED_PAD src0_sel:WORD_1 src1_sel:DWORD
	v_exp_f32_e32 v9, v9
	v_add3_u32 v8, v8, v10, s33
	v_lshrrev_b32_e32 v5, 16, v5
	v_and_or_b32 v8, v8, s2, v5
	v_lshlrev_b32_e32 v5, 16, v95
	v_mul_f32_e32 v5, 0x3db504f3, v5
	v_add_f32_e32 v10, v45, v44
	v_mul_f32_e32 v5, v9, v5
	v_mul_f32_e32 v10, 0x3fb8aa3b, v10
	v_rcp_f32_e32 v11, v9
	v_bfe_u32 v9, v5, 16, 1
	v_exp_f32_e32 v12, v10
	v_add3_u32 v5, v5, v9, s33
	ds_write_b16_d16_hi v77, v5 offset:3808
	v_lshlrev_b32_e32 v5, 16, v96
	v_mul_f32_e32 v5, 0x3db504f3, v5
	v_mul_f32_e32 v5, v12, v5
	v_bfe_u32 v9, v5, 16, 1
	v_rcp_f32_e32 v10, v12
	v_add3_u32 v5, v5, v9, s33
	s_waitcnt lgkmcnt(12)
	v_lshlrev_b32_e32 v13, 16, v101
	ds_write_b16_d16_hi v77, v5 offset:4080
	v_mul_f32_e32 v5, v11, v13
	v_bfe_u32 v9, v5, 16, 1
	s_waitcnt lgkmcnt(12)
	v_lshlrev_b32_e32 v12, 16, v102
	v_add3_u32 v5, v5, v9, s33
	ds_write_b16_d16_hi v77, v5 offset:21216
	v_mul_f32_e32 v5, v10, v12
	v_bfe_u32 v9, v5, 16, 1
	v_add3_u32 v5, v5, v9, s33
	v_pk_mul_f32 v[10:11], v[4:5], v[10:11] op_sel_hi:[0,1]
	v_pk_mul_f32 v[10:11], v[10:11], v[12:13]
	ds_write_b16_d16_hi v77, v5 offset:21488
	v_and_b32_sdwa v5, v11, v188 dst_sel:DWORD dst_unused:UNUSED_PAD src0_sel:WORD_1 src1_sel:DWORD
	v_and_b32_sdwa v9, v10, v188 dst_sel:DWORD dst_unused:UNUSED_PAD src0_sel:WORD_1 src1_sel:DWORD
	v_add3_u32 v5, v11, v5, s33
	v_add3_u32 v9, v10, v9, s33
	v_lshrrev_b32_e32 v5, 16, v5
	v_and_or_b32 v9, v9, s2, v5
	ds_write_b128 v78, v[0:3] offset:34816
	ds_write_b128 v78, v[6:9] offset:34832
	s_and_saveexec_b64 s[2:3], s[12:13]
	s_cbranch_execz .LBB0_352
	global_store_dword v[42:43], v4, off nt
.LBB0_352:
	s_or_b64 exec, exec, s[2:3]
	s_ashr_i32 s2, s41, 5
	s_and_b32 s2, s2, -4
	s_or_b32 s2, s2, s30
	s_ashr_i32 s3, s2, 31
	s_and_b32 s31, s41, 31
	s_lshl_b64 s[34:35], s[2:3], 19
	s_waitcnt lgkmcnt(0)
	s_barrier
	s_add_u32 s30, s36, s34
	ds_read_b128 v[0:3], v88
	s_addc_u32 s35, s37, s35
	s_lshl_b32 s34, s31, 14
	s_add_u32 s34, s30, s34
	s_addc_u32 s35, s35, 0
	v_lshl_add_u64 v[4:5], v[30:31], 1, s[34:35]
	s_waitcnt lgkmcnt(0)
	global_store_dwordx4 v[4:5], v[0:3], off nt
	ds_read_b128 v[0:3], v89
	v_lshl_add_u64 v[4:5], v[34:35], 1, s[34:35]
	v_readlane_b32 s34, v253, 13
	v_readlane_b32 s35, v253, 14
	s_andn2_b64 vcc, exec, s[34:35]
	s_waitcnt lgkmcnt(0)
	global_store_dwordx4 v[4:5], v[0:3], off nt
	v_mov_b32_e32 v4, 0
	v_mov_b32_e32 v5, 0
	v_mov_b32_e32 v0, 0
	v_mov_b32_e32 v2, 0
	v_mov_b32_e32 v3, 0
	s_cbranch_vccnz .LBB0_354
	ds_read_b128 v[2:5], v90
	v_add_u32_e32 v1, v68, v67
	ds_read_b128 v[6:9], v1 offset:17408
	s_waitcnt lgkmcnt(0)
	v_mfma_f32_16x16x32_bf16 v[2:5], v[2:5], v[6:9], 0
	ds_read_b128 v[6:9], v90 offset:64
	ds_read_b128 v[10:13], v1 offset:17472
	s_waitcnt lgkmcnt(0)
	v_mfma_f32_16x16x32_bf16 v[2:5], v[6:9], v[10:13], v[2:5]
	ds_read_b128 v[6:9], v90 offset:128
	ds_read_b128 v[10:13], v1 offset:17536
	s_waitcnt lgkmcnt(0)
	v_mfma_f32_16x16x32_bf16 v[2:5], v[6:9], v[10:13], v[2:5]
	ds_read_b128 v[6:9], v90 offset:192
	ds_read_b128 v[10:13], v1 offset:17600
	s_waitcnt lgkmcnt(0)
	v_mfma_f32_16x16x32_bf16 v[2:5], v[6:9], v[10:13], v[2:5]
